# speedup vs baseline: 1.0049x; 1.0049x over previous
.LBB3_11:
	s_lshl_b32 s58, s42, 7
	s_add_i32 s59, s41, 0x400
	s_lshr_b32 s59, s59, 6
	s_bfe_u32 s60, s20, 0x1000c
	s_add_i32 s59, s59, s60
	s_lshl_b32 s59, s59, 19
	s_add_u32 s58, s58, s59
	s_add_u32 s58, s56, s58
	s_addc_u32 s59, s57, 0
	s_add_u32 s60, s58, 0x4000
	s_addc_u32 s61, s59, 0
	s_add_u32 s62, s58, 0x100000
	s_addc_u32 s63, s59, 0
	s_add_u32 s64, s62, 0x4000
	s_addc_u32 s65, s63, 0
	s_lshr_b32 s66, s41, 7
	s_bfe_u32 s67, s20, 0x1000c
	s_add_i32 s66, s66, s67
	s_lshl_b32 s66, s66, 14
	s_lshl_b32 s67, s42, 2
	s_add_u32 s66, s66, s67
	s_add_u32 s66, s14, s66
	s_addc_u32 s67, s15, 0
	v_add_u32_e32 v172, s43, v207
	v_pk_fma_f32 v[244:245], v[244:245], -0.5, -0.5 op_sel_hi:[1,0,0]
	v_pk_fma_f32 v[246:247], v[246:247], -0.5, -0.5 op_sel_hi:[1,0,0]
	v_pk_fma_f32 v[248:249], v[248:249], -0.5, -0.5 op_sel_hi:[1,0,0]
	v_pk_fma_f32 v[250:251], v[250:251], -0.5, -0.5 op_sel_hi:[1,0,0]
	v_pk_fma_f32 v[252:253], v[252:253], -0.5, -0.5 op_sel_hi:[1,0,0]
	v_pk_fma_f32 v[254:255], v[254:255], -0.5, -0.5 op_sel_hi:[1,0,0]
	v_pk_fma_f32 v[232:233], v[232:233], -0.5, -0.5 op_sel_hi:[1,0,0]
	v_pk_fma_f32 v[234:235], v[234:235], -0.5, -0.5 op_sel_hi:[1,0,0]
	v_pk_mul_f32 v[134:135], v[244:245], v[246:247]
	v_pk_mul_f32 v[146:147], v[248:249], v[250:251]
	v_pk_mul_f32 v[180:181], v[252:253], v[254:255]
	v_pk_mul_f32 v[236:237], v[232:233], v[234:235]
	v_mul_f32_e32 v188, v134, v135
	v_mul_f32_e32 v190, v146, v147
	v_mul_f32_e32 v189, v180, v181
	v_mul_f32_e32 v191, v236, v237
	v_pk_mul_f32 v[192:193], v[188:189], v[190:191]
	v_mul_f32_e32 v162, v192, v193
	v_rcp_f32_e32 v173, v162
	v_pk_add_f32 v[164:165], v[114:115], v[116:117]
	v_pk_add_f32 v[164:165], v[164:165], v[78:79]
	v_pk_add_f32 v[164:165], v[164:165], v[80:81]
	v_pk_add_f32 v[164:165], v[164:165], v[106:107]
	v_pk_add_f32 v[164:165], v[164:165], v[108:109]
	v_pk_add_f32 v[164:165], v[164:165], v[70:71]
	v_pk_add_f32 v[164:165], v[164:165], v[72:73]
	v_pk_mul_f32 v[230:231], v[172:173], v[192:193] op_sel:[1,1] op_sel_hi:[1,0]
	v_pk_mul_f32 v[192:193], v[230:231], v[190:191]
	v_pk_mul_f32 v[190:191], v[230:231], v[188:189]
	v_pk_mul_f32 v[136:137], v[192:193], v[134:135] op_sel:[0,1] op_sel_hi:[0,0]
	v_pk_mul_f32 v[148:149], v[190:191], v[146:147] op_sel:[0,1] op_sel_hi:[0,0]
	v_pk_mul_f32 v[182:183], v[192:193], v[180:181] op_sel:[1,1] op_sel_hi:[1,0]
	v_pk_mul_f32 v[238:239], v[190:191], v[236:237] op_sel:[1,1] op_sel_hi:[1,0]
	v_pk_fma_f32 v[138:139], v[136:137], v[246:247], 1.0 op_sel_hi:[1,1,0]
	v_pk_fma_f32 v[140:141], v[136:137], v[244:245], 1.0 op_sel_hi:[1,1,0]
	v_pk_fma_f32 v[150:151], v[148:149], v[250:251], 1.0 op_sel_hi:[1,1,0]
	v_pk_fma_f32 v[152:153], v[148:149], v[248:249], 1.0 op_sel_hi:[1,1,0]
	v_pk_fma_f32 v[184:185], v[182:183], v[254:255], 1.0 op_sel_hi:[1,1,0]
	v_pk_fma_f32 v[186:187], v[182:183], v[252:253], 1.0 op_sel_hi:[1,1,0]
	v_pk_fma_f32 v[240:241], v[238:239], v[234:235], 1.0 op_sel_hi:[1,1,0]
	v_pk_fma_f32 v[242:243], v[238:239], v[232:233], 1.0 op_sel_hi:[1,1,0]
	v_cvt_pk_bf16_f32 v154, v138, v139
	v_cvt_pk_bf16_f32 v155, v140, v141
	v_cvt_pk_bf16_f32 v156, v150, v151
	v_cvt_pk_bf16_f32 v157, v152, v153
	v_cvt_pk_bf16_f32 v158, v184, v185
	v_cvt_pk_bf16_f32 v159, v186, v187
	v_cvt_pk_bf16_f32 v160, v240, v241
	v_cvt_pk_bf16_f32 v161, v242, v243
	ds_read_b128 v[114:117], v172
	ds_read_b128 v[78:81], v172 offset:64
	ds_read_b128 v[106:109], v172 offset:128
	ds_read_b128 v[70:73], v172 offset:192
	v_permlane16_swap_b32_e32 v154, v156
	v_permlane16_swap_b32_e32 v155, v157
	global_store_dwordx4 v228, v[154:157], s[58:59] nt
	s_bitcmp1_b32 s20, 12
	s_cbranch_scc1 .Lg1_noX
	s_barrier
.Lg1_noX:
	v_permlane16_swap_b32_e32 v158, v160
	v_permlane16_swap_b32_e32 v159, v161
	global_store_dwordx4 v228, v[158:161], s[58:59] offset:128 nt
	v_exp_f32_e32 v130, v90
	v_exp_f32_e32 v131, v91
	v_exp_f32_e32 v132, v92
	v_exp_f32_e32 v133, v93
	v_exp_f32_e32 v142, v42
	v_exp_f32_e32 v143, v43
	v_exp_f32_e32 v144, v44
	v_exp_f32_e32 v145, v45
	v_exp_f32_e32 v176, v126
	v_exp_f32_e32 v177, v127
	v_exp_f32_e32 v178, v128
	v_exp_f32_e32 v179, v129
	v_exp_f32_e32 v232, v58
	v_exp_f32_e32 v233, v59
	v_exp_f32_e32 v234, v60
	v_exp_f32_e32 v235, v61
	v_pk_fma_f32 v[130:131], v[130:131], -0.5, -0.5 op_sel_hi:[1,0,0]
	v_pk_fma_f32 v[132:133], v[132:133], -0.5, -0.5 op_sel_hi:[1,0,0]
	v_pk_fma_f32 v[142:143], v[142:143], -0.5, -0.5 op_sel_hi:[1,0,0]
	v_pk_fma_f32 v[144:145], v[144:145], -0.5, -0.5 op_sel_hi:[1,0,0]
	v_pk_fma_f32 v[176:177], v[176:177], -0.5, -0.5 op_sel_hi:[1,0,0]
	v_pk_fma_f32 v[178:179], v[178:179], -0.5, -0.5 op_sel_hi:[1,0,0]
	v_pk_fma_f32 v[232:233], v[232:233], -0.5, -0.5 op_sel_hi:[1,0,0]
	v_pk_fma_f32 v[234:235], v[234:235], -0.5, -0.5 op_sel_hi:[1,0,0]
	v_pk_mul_f32 v[134:135], v[130:131], v[132:133]
	v_pk_mul_f32 v[146:147], v[142:143], v[144:145]
	v_pk_mul_f32 v[180:181], v[176:177], v[178:179]
	v_pk_mul_f32 v[236:237], v[232:233], v[234:235]
	v_mul_f32_e32 v188, v134, v135
	v_mul_f32_e32 v190, v146, v147
	v_mul_f32_e32 v189, v180, v181
	v_mul_f32_e32 v191, v236, v237
	v_pk_mul_f32 v[192:193], v[188:189], v[190:191]
	v_mul_f32_e32 v174, v192, v193
	v_rcp_f32_e32 v173, v174
	v_pk_add_f32 v[164:165], v[164:165], v[90:91]
	v_pk_add_f32 v[164:165], v[164:165], v[92:93]
	v_pk_add_f32 v[164:165], v[164:165], v[42:43]
	v_pk_add_f32 v[164:165], v[164:165], v[44:45]
	v_pk_add_f32 v[164:165], v[164:165], v[126:127]
	v_pk_add_f32 v[164:165], v[164:165], v[128:129]
	v_pk_add_f32 v[164:165], v[164:165], v[58:59]
	v_pk_add_f32 v[164:165], v[164:165], v[60:61]
	v_pk_mul_f32 v[230:231], v[172:173], v[192:193] op_sel:[1,1] op_sel_hi:[1,0]
	v_pk_mul_f32 v[192:193], v[230:231], v[190:191]
	v_pk_mul_f32 v[190:191], v[230:231], v[188:189]
	v_pk_mul_f32 v[136:137], v[192:193], v[134:135] op_sel:[0,1] op_sel_hi:[0,0]
	v_pk_mul_f32 v[148:149], v[190:191], v[146:147] op_sel:[0,1] op_sel_hi:[0,0]
	v_pk_mul_f32 v[182:183], v[192:193], v[180:181] op_sel:[1,1] op_sel_hi:[1,0]
	v_pk_mul_f32 v[238:239], v[190:191], v[236:237] op_sel:[1,1] op_sel_hi:[1,0]
	v_pk_fma_f32 v[138:139], v[136:137], v[132:133], 1.0 op_sel_hi:[1,1,0]
	v_pk_fma_f32 v[140:141], v[136:137], v[130:131], 1.0 op_sel_hi:[1,1,0]
	v_pk_fma_f32 v[150:151], v[148:149], v[144:145], 1.0 op_sel_hi:[1,1,0]
	v_pk_fma_f32 v[152:153], v[148:149], v[142:143], 1.0 op_sel_hi:[1,1,0]
	v_pk_fma_f32 v[184:185], v[182:183], v[178:179], 1.0 op_sel_hi:[1,1,0]
	v_pk_fma_f32 v[186:187], v[182:183], v[176:177], 1.0 op_sel_hi:[1,1,0]
	v_pk_fma_f32 v[240:241], v[238:239], v[234:235], 1.0 op_sel_hi:[1,1,0]
	v_pk_fma_f32 v[242:243], v[238:239], v[232:233], 1.0 op_sel_hi:[1,1,0]
	v_cvt_pk_bf16_f32 v154, v138, v139
	v_cvt_pk_bf16_f32 v155, v140, v141
	v_cvt_pk_bf16_f32 v156, v150, v151
	v_cvt_pk_bf16_f32 v157, v152, v153
	v_cvt_pk_bf16_f32 v158, v184, v185
	v_cvt_pk_bf16_f32 v159, v186, v187
	v_cvt_pk_bf16_f32 v160, v240, v241
	v_cvt_pk_bf16_f32 v161, v242, v243
	ds_read_b128 v[90:93], v172 offset:512
	ds_read_b128 v[42:45], v172 offset:576
	ds_read_b128 v[126:129], v172 offset:640
	ds_read_b128 v[58:61], v172 offset:704
	v_permlane16_swap_b32_e32 v154, v156
	v_permlane16_swap_b32_e32 v155, v157
	global_store_dwordx4 v228, v[154:157], s[62:63] nt
	v_permlane16_swap_b32_e32 v158, v160
	v_permlane16_swap_b32_e32 v159, v161
	global_store_dwordx4 v228, v[158:161], s[62:63] offset:128 nt
	v_log_f32_e32 v166, v162
	v_log_f32_e32 v170, v174
	v_add_f32_e32 v168, v164, v165
	v_mul_f32_e32 v168, 0xbeb17218, v168
	v_add_f32_e32 v166, v166, v170
	v_fmac_f32_e32 v168, 0x3f317218, v166
	v_mov_b32_e32 v169, v168
	s_nop 1
	v_permlane16_swap_b32_e32 v168, v169
	v_add_f32_e32 v168, v168, v169
	v_mov_b32_e32 v169, v168
	s_nop 1
	v_permlane32_swap_b32_e32 v168, v169
	v_add_f32_e32 v168, v168, v169
	s_mov_b64 exec, s[0:1]
	global_store_dword v229, v168, s[66:67]
	s_mov_b64 exec, -1
	v_exp_f32_e32 v130, v110
	v_exp_f32_e32 v131, v111
	v_exp_f32_e32 v132, v112
	v_exp_f32_e32 v133, v113
	v_exp_f32_e32 v142, v74
	v_exp_f32_e32 v143, v75
	v_exp_f32_e32 v144, v76
	v_exp_f32_e32 v145, v77
	v_exp_f32_e32 v176, v102
	v_exp_f32_e32 v177, v103
	v_exp_f32_e32 v178, v104
	v_exp_f32_e32 v179, v105
	v_exp_f32_e32 v232, v66
	v_exp_f32_e32 v233, v67
	v_exp_f32_e32 v234, v68
	v_exp_f32_e32 v235, v69
	v_pk_fma_f32 v[130:131], v[130:131], -0.5, -0.5 op_sel_hi:[1,0,0]
	v_pk_fma_f32 v[132:133], v[132:133], -0.5, -0.5 op_sel_hi:[1,0,0]
	v_pk_fma_f32 v[142:143], v[142:143], -0.5, -0.5 op_sel_hi:[1,0,0]
	v_pk_fma_f32 v[144:145], v[144:145], -0.5, -0.5 op_sel_hi:[1,0,0]
	v_pk_fma_f32 v[176:177], v[176:177], -0.5, -0.5 op_sel_hi:[1,0,0]
	v_pk_fma_f32 v[178:179], v[178:179], -0.5, -0.5 op_sel_hi:[1,0,0]
	v_pk_fma_f32 v[232:233], v[232:233], -0.5, -0.5 op_sel_hi:[1,0,0]
	v_pk_fma_f32 v[234:235], v[234:235], -0.5, -0.5 op_sel_hi:[1,0,0]
	v_pk_mul_f32 v[134:135], v[130:131], v[132:133]
	v_pk_mul_f32 v[146:147], v[142:143], v[144:145]
	v_pk_mul_f32 v[180:181], v[176:177], v[178:179]
	v_pk_mul_f32 v[236:237], v[232:233], v[234:235]
	v_mul_f32_e32 v188, v134, v135
	v_mul_f32_e32 v190, v146, v147
	v_mul_f32_e32 v189, v180, v181
	v_mul_f32_e32 v191, v236, v237
	v_pk_mul_f32 v[192:193], v[188:189], v[190:191]
	v_mul_f32_e32 v162, v192, v193
	v_rcp_f32_e32 v173, v162
	v_pk_add_f32 v[164:165], v[110:111], v[112:113]
	v_pk_add_f32 v[164:165], v[164:165], v[74:75]
	v_pk_add_f32 v[164:165], v[164:165], v[76:77]
	v_pk_add_f32 v[164:165], v[164:165], v[102:103]
	v_pk_add_f32 v[164:165], v[164:165], v[104:105]
	v_pk_add_f32 v[164:165], v[164:165], v[66:67]
	v_pk_add_f32 v[164:165], v[164:165], v[68:69]
	v_pk_mul_f32 v[230:231], v[172:173], v[192:193] op_sel:[1,1] op_sel_hi:[1,0]
	v_pk_mul_f32 v[192:193], v[230:231], v[190:191]
	v_pk_mul_f32 v[190:191], v[230:231], v[188:189]
	v_pk_mul_f32 v[136:137], v[192:193], v[134:135] op_sel:[0,1] op_sel_hi:[0,0]
	v_pk_mul_f32 v[148:149], v[190:191], v[146:147] op_sel:[0,1] op_sel_hi:[0,0]
	v_pk_mul_f32 v[182:183], v[192:193], v[180:181] op_sel:[1,1] op_sel_hi:[1,0]
	v_pk_mul_f32 v[238:239], v[190:191], v[236:237] op_sel:[1,1] op_sel_hi:[1,0]
	v_pk_fma_f32 v[138:139], v[136:137], v[132:133], 1.0 op_sel_hi:[1,1,0]
	v_pk_fma_f32 v[140:141], v[136:137], v[130:131], 1.0 op_sel_hi:[1,1,0]
	v_pk_fma_f32 v[150:151], v[148:149], v[144:145], 1.0 op_sel_hi:[1,1,0]
	v_pk_fma_f32 v[152:153], v[148:149], v[142:143], 1.0 op_sel_hi:[1,1,0]
	v_pk_fma_f32 v[184:185], v[182:183], v[178:179], 1.0 op_sel_hi:[1,1,0]
	v_pk_fma_f32 v[186:187], v[182:183], v[176:177], 1.0 op_sel_hi:[1,1,0]
	v_pk_fma_f32 v[240:241], v[238:239], v[234:235], 1.0 op_sel_hi:[1,1,0]
	v_pk_fma_f32 v[242:243], v[238:239], v[232:233], 1.0 op_sel_hi:[1,1,0]
	v_cvt_pk_bf16_f32 v154, v138, v139
	v_cvt_pk_bf16_f32 v155, v140, v141
	v_cvt_pk_bf16_f32 v156, v150, v151
	v_cvt_pk_bf16_f32 v157, v152, v153
	v_cvt_pk_bf16_f32 v158, v184, v185
	v_cvt_pk_bf16_f32 v159, v186, v187
	v_cvt_pk_bf16_f32 v160, v240, v241
	v_cvt_pk_bf16_f32 v161, v242, v243
	ds_read_b128 v[110:113], v172
	ds_read_b128 v[74:77], v172 offset:64
	ds_read_b128 v[102:105], v172 offset:128
	ds_read_b128 v[66:69], v172 offset:192
	v_permlane16_swap_b32_e32 v154, v156
	v_permlane16_swap_b32_e32 v155, v157
	global_store_dwordx4 v228, v[154:157], s[58:59] offset:2048 nt
	v_permlane16_swap_b32_e32 v158, v160
	v_permlane16_swap_b32_e32 v159, v161
	global_store_dwordx4 v228, v[158:161], s[58:59] offset:2176 nt
	v_exp_f32_e32 v130, v86
	v_exp_f32_e32 v131, v87
	v_exp_f32_e32 v132, v88
	v_exp_f32_e32 v133, v89
	v_exp_f32_e32 v142, v38
	v_exp_f32_e32 v143, v39
	v_exp_f32_e32 v144, v40
	v_exp_f32_e32 v145, v41
	v_exp_f32_e32 v176, v122
	v_exp_f32_e32 v177, v123
	v_exp_f32_e32 v178, v124
	v_exp_f32_e32 v179, v125
	v_exp_f32_e32 v232, v50
	v_exp_f32_e32 v233, v51
	v_exp_f32_e32 v234, v52
	v_exp_f32_e32 v235, v53
	v_pk_fma_f32 v[130:131], v[130:131], -0.5, -0.5 op_sel_hi:[1,0,0]
	v_pk_fma_f32 v[132:133], v[132:133], -0.5, -0.5 op_sel_hi:[1,0,0]
	v_pk_fma_f32 v[142:143], v[142:143], -0.5, -0.5 op_sel_hi:[1,0,0]
	v_pk_fma_f32 v[144:145], v[144:145], -0.5, -0.5 op_sel_hi:[1,0,0]
	v_pk_fma_f32 v[176:177], v[176:177], -0.5, -0.5 op_sel_hi:[1,0,0]
	v_pk_fma_f32 v[178:179], v[178:179], -0.5, -0.5 op_sel_hi:[1,0,0]
	v_pk_fma_f32 v[232:233], v[232:233], -0.5, -0.5 op_sel_hi:[1,0,0]
	v_pk_fma_f32 v[234:235], v[234:235], -0.5, -0.5 op_sel_hi:[1,0,0]
	v_pk_mul_f32 v[134:135], v[130:131], v[132:133]
	v_pk_mul_f32 v[146:147], v[142:143], v[144:145]
	v_pk_mul_f32 v[180:181], v[176:177], v[178:179]
	v_pk_mul_f32 v[236:237], v[232:233], v[234:235]
	v_mul_f32_e32 v188, v134, v135
	v_mul_f32_e32 v190, v146, v147
	v_mul_f32_e32 v189, v180, v181
	v_mul_f32_e32 v191, v236, v237
	v_pk_mul_f32 v[192:193], v[188:189], v[190:191]
	v_mul_f32_e32 v174, v192, v193
	v_rcp_f32_e32 v173, v174
	v_pk_add_f32 v[164:165], v[164:165], v[86:87]
	v_pk_add_f32 v[164:165], v[164:165], v[88:89]
	v_pk_add_f32 v[164:165], v[164:165], v[38:39]
	v_pk_add_f32 v[164:165], v[164:165], v[40:41]
	v_pk_add_f32 v[164:165], v[164:165], v[122:123]
	v_pk_add_f32 v[164:165], v[164:165], v[124:125]
	v_pk_add_f32 v[164:165], v[164:165], v[50:51]
	v_pk_add_f32 v[164:165], v[164:165], v[52:53]
	v_pk_mul_f32 v[230:231], v[172:173], v[192:193] op_sel:[1,1] op_sel_hi:[1,0]
	v_pk_mul_f32 v[192:193], v[230:231], v[190:191]
	v_pk_mul_f32 v[190:191], v[230:231], v[188:189]
	v_pk_mul_f32 v[136:137], v[192:193], v[134:135] op_sel:[0,1] op_sel_hi:[0,0]
	v_pk_mul_f32 v[148:149], v[190:191], v[146:147] op_sel:[0,1] op_sel_hi:[0,0]
	v_pk_mul_f32 v[182:183], v[192:193], v[180:181] op_sel:[1,1] op_sel_hi:[1,0]
	v_pk_mul_f32 v[238:239], v[190:191], v[236:237] op_sel:[1,1] op_sel_hi:[1,0]
	v_pk_fma_f32 v[138:139], v[136:137], v[132:133], 1.0 op_sel_hi:[1,1,0]
	v_pk_fma_f32 v[140:141], v[136:137], v[130:131], 1.0 op_sel_hi:[1,1,0]
	v_pk_fma_f32 v[150:151], v[148:149], v[144:145], 1.0 op_sel_hi:[1,1,0]
	v_pk_fma_f32 v[152:153], v[148:149], v[142:143], 1.0 op_sel_hi:[1,1,0]
	v_pk_fma_f32 v[184:185], v[182:183], v[178:179], 1.0 op_sel_hi:[1,1,0]
	v_pk_fma_f32 v[186:187], v[182:183], v[176:177], 1.0 op_sel_hi:[1,1,0]
	v_pk_fma_f32 v[240:241], v[238:239], v[234:235], 1.0 op_sel_hi:[1,1,0]
	v_pk_fma_f32 v[242:243], v[238:239], v[232:233], 1.0 op_sel_hi:[1,1,0]
	v_cvt_pk_bf16_f32 v154, v138, v139
	v_cvt_pk_bf16_f32 v155, v140, v141
	v_cvt_pk_bf16_f32 v156, v150, v151
	v_cvt_pk_bf16_f32 v157, v152, v153
	v_cvt_pk_bf16_f32 v158, v184, v185
	v_cvt_pk_bf16_f32 v159, v186, v187
	v_cvt_pk_bf16_f32 v160, v240, v241
	v_cvt_pk_bf16_f32 v161, v242, v243
	ds_read_b128 v[86:89], v172 offset:512
	ds_read_b128 v[38:41], v172 offset:576
	ds_read_b128 v[122:125], v172 offset:640
	ds_read_b128 v[50:53], v172 offset:704
	v_permlane16_swap_b32_e32 v154, v156
	v_permlane16_swap_b32_e32 v155, v157
	global_store_dwordx4 v228, v[154:157], s[62:63] offset:2048 nt
	v_permlane16_swap_b32_e32 v158, v160
	v_permlane16_swap_b32_e32 v159, v161
	global_store_dwordx4 v228, v[158:161], s[62:63] offset:2176 nt
	v_log_f32_e32 v166, v162
	v_log_f32_e32 v170, v174
	v_add_f32_e32 v168, v164, v165
	v_mul_f32_e32 v168, 0xbeb17218, v168
	v_add_f32_e32 v166, v166, v170
	v_fmac_f32_e32 v168, 0x3f317218, v166
	v_mov_b32_e32 v169, v168
	s_nop 1
	v_permlane16_swap_b32_e32 v168, v169
	v_add_f32_e32 v168, v168, v169
	v_mov_b32_e32 v169, v168
	s_nop 1
	v_permlane32_swap_b32_e32 v168, v169
	v_add_f32_e32 v168, v168, v169
	s_mov_b64 exec, s[0:1]
	global_store_dword v229, v168, s[66:67] offset:64
	s_mov_b64 exec, -1
	v_exp_f32_e32 v130, v98
	v_exp_f32_e32 v131, v99
	v_exp_f32_e32 v132, v100
	v_exp_f32_e32 v133, v101
	v_exp_f32_e32 v142, v62
	v_exp_f32_e32 v143, v63
	v_exp_f32_e32 v144, v64
	v_exp_f32_e32 v145, v65
	v_exp_f32_e32 v176, v94
	v_exp_f32_e32 v177, v95
	v_exp_f32_e32 v178, v96
	v_exp_f32_e32 v179, v97
	v_exp_f32_e32 v232, v54
	v_exp_f32_e32 v233, v55
	v_exp_f32_e32 v234, v56
	v_exp_f32_e32 v235, v57
	v_pk_fma_f32 v[130:131], v[130:131], -0.5, -0.5 op_sel_hi:[1,0,0]
	v_pk_fma_f32 v[132:133], v[132:133], -0.5, -0.5 op_sel_hi:[1,0,0]
	v_pk_fma_f32 v[142:143], v[142:143], -0.5, -0.5 op_sel_hi:[1,0,0]
	v_pk_fma_f32 v[144:145], v[144:145], -0.5, -0.5 op_sel_hi:[1,0,0]
	v_pk_fma_f32 v[176:177], v[176:177], -0.5, -0.5 op_sel_hi:[1,0,0]
	v_pk_fma_f32 v[178:179], v[178:179], -0.5, -0.5 op_sel_hi:[1,0,0]
	v_pk_fma_f32 v[232:233], v[232:233], -0.5, -0.5 op_sel_hi:[1,0,0]
	v_pk_fma_f32 v[234:235], v[234:235], -0.5, -0.5 op_sel_hi:[1,0,0]
	v_pk_mul_f32 v[134:135], v[130:131], v[132:133]
	v_pk_mul_f32 v[146:147], v[142:143], v[144:145]
	v_pk_mul_f32 v[180:181], v[176:177], v[178:179]
	v_pk_mul_f32 v[236:237], v[232:233], v[234:235]
	v_mul_f32_e32 v188, v134, v135
	v_mul_f32_e32 v190, v146, v147
	v_mul_f32_e32 v189, v180, v181
	v_mul_f32_e32 v191, v236, v237
	v_pk_mul_f32 v[192:193], v[188:189], v[190:191]
	v_mul_f32_e32 v162, v192, v193
	v_rcp_f32_e32 v173, v162
	v_pk_add_f32 v[164:165], v[98:99], v[100:101]
	v_pk_add_f32 v[164:165], v[164:165], v[62:63]
	v_pk_add_f32 v[164:165], v[164:165], v[64:65]
	v_pk_add_f32 v[164:165], v[164:165], v[94:95]
	v_pk_add_f32 v[164:165], v[164:165], v[96:97]
	v_pk_add_f32 v[164:165], v[164:165], v[54:55]
	v_pk_add_f32 v[164:165], v[164:165], v[56:57]
	v_pk_mul_f32 v[230:231], v[172:173], v[192:193] op_sel:[1,1] op_sel_hi:[1,0]
	v_pk_mul_f32 v[192:193], v[230:231], v[190:191]
	v_pk_mul_f32 v[190:191], v[230:231], v[188:189]
	v_pk_mul_f32 v[136:137], v[192:193], v[134:135] op_sel:[0,1] op_sel_hi:[0,0]
	v_pk_mul_f32 v[148:149], v[190:191], v[146:147] op_sel:[0,1] op_sel_hi:[0,0]
	v_pk_mul_f32 v[182:183], v[192:193], v[180:181] op_sel:[1,1] op_sel_hi:[1,0]
	v_pk_mul_f32 v[238:239], v[190:191], v[236:237] op_sel:[1,1] op_sel_hi:[1,0]
	v_pk_fma_f32 v[138:139], v[136:137], v[132:133], 1.0 op_sel_hi:[1,1,0]
	v_pk_fma_f32 v[140:141], v[136:137], v[130:131], 1.0 op_sel_hi:[1,1,0]
	v_pk_fma_f32 v[150:151], v[148:149], v[144:145], 1.0 op_sel_hi:[1,1,0]
	v_pk_fma_f32 v[152:153], v[148:149], v[142:143], 1.0 op_sel_hi:[1,1,0]
	v_pk_fma_f32 v[184:185], v[182:183], v[178:179], 1.0 op_sel_hi:[1,1,0]
	v_pk_fma_f32 v[186:187], v[182:183], v[176:177], 1.0 op_sel_hi:[1,1,0]
	v_pk_fma_f32 v[240:241], v[238:239], v[234:235], 1.0 op_sel_hi:[1,1,0]
	v_pk_fma_f32 v[242:243], v[238:239], v[232:233], 1.0 op_sel_hi:[1,1,0]
	v_cvt_pk_bf16_f32 v154, v138, v139
	v_cvt_pk_bf16_f32 v155, v140, v141
	v_cvt_pk_bf16_f32 v156, v150, v151
	v_cvt_pk_bf16_f32 v157, v152, v153
	v_cvt_pk_bf16_f32 v158, v184, v185
	v_cvt_pk_bf16_f32 v159, v186, v187
	v_cvt_pk_bf16_f32 v160, v240, v241
	v_cvt_pk_bf16_f32 v161, v242, v243
	ds_read_b128 v[98:101], v172
	ds_read_b128 v[62:65], v172 offset:64
	ds_read_b128 v[94:97], v172 offset:128
	ds_read_b128 v[54:57], v172 offset:192
	v_permlane16_swap_b32_e32 v154, v156
	v_permlane16_swap_b32_e32 v155, v157
	global_store_dwordx4 v228, v[154:157], s[60:61] nt
	v_permlane16_swap_b32_e32 v158, v160
	v_permlane16_swap_b32_e32 v159, v161
	global_store_dwordx4 v228, v[158:161], s[60:61] offset:128 nt
	v_exp_f32_e32 v130, v82
	v_exp_f32_e32 v131, v83
	v_exp_f32_e32 v132, v84
	v_exp_f32_e32 v133, v85
	v_exp_f32_e32 v142, v34
	v_exp_f32_e32 v143, v35
	v_exp_f32_e32 v144, v36
	v_exp_f32_e32 v145, v37
	v_exp_f32_e32 v176, v118
	v_exp_f32_e32 v177, v119
	v_exp_f32_e32 v178, v120
	v_exp_f32_e32 v179, v121
	v_exp_f32_e32 v232, v46
	v_exp_f32_e32 v233, v47
	v_exp_f32_e32 v234, v48
	v_exp_f32_e32 v235, v49
	v_pk_fma_f32 v[130:131], v[130:131], -0.5, -0.5 op_sel_hi:[1,0,0]
	v_pk_fma_f32 v[132:133], v[132:133], -0.5, -0.5 op_sel_hi:[1,0,0]
	v_pk_fma_f32 v[142:143], v[142:143], -0.5, -0.5 op_sel_hi:[1,0,0]
	v_pk_fma_f32 v[144:145], v[144:145], -0.5, -0.5 op_sel_hi:[1,0,0]
	v_pk_fma_f32 v[176:177], v[176:177], -0.5, -0.5 op_sel_hi:[1,0,0]
	v_pk_fma_f32 v[178:179], v[178:179], -0.5, -0.5 op_sel_hi:[1,0,0]
	v_pk_fma_f32 v[232:233], v[232:233], -0.5, -0.5 op_sel_hi:[1,0,0]
	v_pk_fma_f32 v[234:235], v[234:235], -0.5, -0.5 op_sel_hi:[1,0,0]
	v_pk_mul_f32 v[134:135], v[130:131], v[132:133]
	v_pk_mul_f32 v[146:147], v[142:143], v[144:145]
	v_pk_mul_f32 v[180:181], v[176:177], v[178:179]
	v_pk_mul_f32 v[236:237], v[232:233], v[234:235]
	v_mul_f32_e32 v188, v134, v135
	v_mul_f32_e32 v190, v146, v147
	v_mul_f32_e32 v189, v180, v181
	v_mul_f32_e32 v191, v236, v237
	v_pk_mul_f32 v[192:193], v[188:189], v[190:191]
	v_mul_f32_e32 v174, v192, v193
	v_rcp_f32_e32 v173, v174
	v_pk_add_f32 v[164:165], v[164:165], v[82:83]
	v_pk_add_f32 v[164:165], v[164:165], v[84:85]
	v_pk_add_f32 v[164:165], v[164:165], v[34:35]
	v_pk_add_f32 v[164:165], v[164:165], v[36:37]
	v_pk_add_f32 v[164:165], v[164:165], v[118:119]
	v_pk_add_f32 v[164:165], v[164:165], v[120:121]
	v_pk_add_f32 v[164:165], v[164:165], v[46:47]
	v_pk_add_f32 v[164:165], v[164:165], v[48:49]
	v_pk_mul_f32 v[230:231], v[172:173], v[192:193] op_sel:[1,1] op_sel_hi:[1,0]
	v_pk_mul_f32 v[192:193], v[230:231], v[190:191]
	v_pk_mul_f32 v[190:191], v[230:231], v[188:189]
	v_pk_mul_f32 v[136:137], v[192:193], v[134:135] op_sel:[0,1] op_sel_hi:[0,0]
	v_pk_mul_f32 v[148:149], v[190:191], v[146:147] op_sel:[0,1] op_sel_hi:[0,0]
	v_pk_mul_f32 v[182:183], v[192:193], v[180:181] op_sel:[1,1] op_sel_hi:[1,0]
	v_pk_mul_f32 v[238:239], v[190:191], v[236:237] op_sel:[1,1] op_sel_hi:[1,0]
	v_pk_fma_f32 v[138:139], v[136:137], v[132:133], 1.0 op_sel_hi:[1,1,0]
	v_pk_fma_f32 v[140:141], v[136:137], v[130:131], 1.0 op_sel_hi:[1,1,0]
	v_pk_fma_f32 v[150:151], v[148:149], v[144:145], 1.0 op_sel_hi:[1,1,0]
	v_pk_fma_f32 v[152:153], v[148:149], v[142:143], 1.0 op_sel_hi:[1,1,0]
	v_pk_fma_f32 v[184:185], v[182:183], v[178:179], 1.0 op_sel_hi:[1,1,0]
	v_pk_fma_f32 v[186:187], v[182:183], v[176:177], 1.0 op_sel_hi:[1,1,0]
	v_pk_fma_f32 v[240:241], v[238:239], v[234:235], 1.0 op_sel_hi:[1,1,0]
	v_pk_fma_f32 v[242:243], v[238:239], v[232:233], 1.0 op_sel_hi:[1,1,0]
	v_cvt_pk_bf16_f32 v154, v138, v139
	v_cvt_pk_bf16_f32 v155, v140, v141
	v_cvt_pk_bf16_f32 v156, v150, v151
	v_cvt_pk_bf16_f32 v157, v152, v153
	v_cvt_pk_bf16_f32 v158, v184, v185
	v_cvt_pk_bf16_f32 v159, v186, v187
	v_cvt_pk_bf16_f32 v160, v240, v241
	v_cvt_pk_bf16_f32 v161, v242, v243
	ds_read_b128 v[82:85], v172 offset:512
	ds_read_b128 v[34:37], v172 offset:576
	ds_read_b128 v[118:121], v172 offset:640
	ds_read_b128 v[46:49], v172 offset:704
	v_permlane16_swap_b32_e32 v154, v156
	v_permlane16_swap_b32_e32 v155, v157
	global_store_dwordx4 v228, v[154:157], s[64:65] nt
	v_permlane16_swap_b32_e32 v158, v160
	v_permlane16_swap_b32_e32 v159, v161
	global_store_dwordx4 v228, v[158:161], s[64:65] offset:128 nt
	v_log_f32_e32 v166, v162
	v_log_f32_e32 v170, v174
	v_add_f32_e32 v168, v164, v165
	v_mul_f32_e32 v168, 0xbeb17218, v168
	v_add_f32_e32 v166, v166, v170
	v_fmac_f32_e32 v168, 0x3f317218, v166
	v_mov_b32_e32 v169, v168
	s_nop 1
	v_permlane16_swap_b32_e32 v168, v169
	v_add_f32_e32 v168, v168, v169
	v_mov_b32_e32 v169, v168
	s_nop 1
	v_permlane32_swap_b32_e32 v168, v169
	v_add_f32_e32 v168, v168, v169
	s_mov_b64 exec, s[0:1]
	global_store_dword v229, v168, s[66:67] offset:512
	s_mov_b64 exec, -1
	v_exp_f32_e32 v130, v18
	v_exp_f32_e32 v131, v19
	v_exp_f32_e32 v132, v20
	v_exp_f32_e32 v133, v21
	v_exp_f32_e32 v142, v2
	v_exp_f32_e32 v143, v3
	v_exp_f32_e32 v144, v4
	v_exp_f32_e32 v145, v5
	v_exp_f32_e32 v176, v26
	v_exp_f32_e32 v177, v27
	v_exp_f32_e32 v178, v28
	v_exp_f32_e32 v179, v29
	v_exp_f32_e32 v232, v10
	v_exp_f32_e32 v233, v11
	v_exp_f32_e32 v234, v12
	v_exp_f32_e32 v235, v13
	v_pk_fma_f32 v[130:131], v[130:131], -0.5, -0.5 op_sel_hi:[1,0,0]
	v_pk_fma_f32 v[132:133], v[132:133], -0.5, -0.5 op_sel_hi:[1,0,0]
	v_pk_fma_f32 v[142:143], v[142:143], -0.5, -0.5 op_sel_hi:[1,0,0]
	v_pk_fma_f32 v[144:145], v[144:145], -0.5, -0.5 op_sel_hi:[1,0,0]
	v_pk_fma_f32 v[176:177], v[176:177], -0.5, -0.5 op_sel_hi:[1,0,0]
	v_pk_fma_f32 v[178:179], v[178:179], -0.5, -0.5 op_sel_hi:[1,0,0]
	v_pk_fma_f32 v[232:233], v[232:233], -0.5, -0.5 op_sel_hi:[1,0,0]
	v_pk_fma_f32 v[234:235], v[234:235], -0.5, -0.5 op_sel_hi:[1,0,0]
	v_pk_mul_f32 v[134:135], v[130:131], v[132:133]
	v_pk_mul_f32 v[146:147], v[142:143], v[144:145]
	v_pk_mul_f32 v[180:181], v[176:177], v[178:179]
	v_pk_mul_f32 v[236:237], v[232:233], v[234:235]
	v_mul_f32_e32 v188, v134, v135
	v_mul_f32_e32 v190, v146, v147
	v_mul_f32_e32 v189, v180, v181
	v_mul_f32_e32 v191, v236, v237
	v_pk_mul_f32 v[192:193], v[188:189], v[190:191]
	v_mul_f32_e32 v162, v192, v193
	v_rcp_f32_e32 v173, v162
	v_pk_add_f32 v[164:165], v[18:19], v[20:21]
	v_pk_add_f32 v[164:165], v[164:165], v[2:3]
	v_pk_add_f32 v[164:165], v[164:165], v[4:5]
	v_pk_add_f32 v[164:165], v[164:165], v[26:27]
	v_pk_add_f32 v[164:165], v[164:165], v[28:29]
	v_pk_add_f32 v[164:165], v[164:165], v[10:11]
	v_pk_add_f32 v[164:165], v[164:165], v[12:13]
	v_pk_mul_f32 v[230:231], v[172:173], v[192:193] op_sel:[1,1] op_sel_hi:[1,0]
	v_pk_mul_f32 v[192:193], v[230:231], v[190:191]
	v_pk_mul_f32 v[190:191], v[230:231], v[188:189]
	v_pk_mul_f32 v[136:137], v[192:193], v[134:135] op_sel:[0,1] op_sel_hi:[0,0]
	v_pk_mul_f32 v[148:149], v[190:191], v[146:147] op_sel:[0,1] op_sel_hi:[0,0]
	v_pk_mul_f32 v[182:183], v[192:193], v[180:181] op_sel:[1,1] op_sel_hi:[1,0]
	v_pk_mul_f32 v[238:239], v[190:191], v[236:237] op_sel:[1,1] op_sel_hi:[1,0]
	v_pk_fma_f32 v[138:139], v[136:137], v[132:133], 1.0 op_sel_hi:[1,1,0]
	v_pk_fma_f32 v[140:141], v[136:137], v[130:131], 1.0 op_sel_hi:[1,1,0]
	v_pk_fma_f32 v[150:151], v[148:149], v[144:145], 1.0 op_sel_hi:[1,1,0]
	v_pk_fma_f32 v[152:153], v[148:149], v[142:143], 1.0 op_sel_hi:[1,1,0]
	v_pk_fma_f32 v[184:185], v[182:183], v[178:179], 1.0 op_sel_hi:[1,1,0]
	v_pk_fma_f32 v[186:187], v[182:183], v[176:177], 1.0 op_sel_hi:[1,1,0]
	v_pk_fma_f32 v[240:241], v[238:239], v[234:235], 1.0 op_sel_hi:[1,1,0]
	v_pk_fma_f32 v[242:243], v[238:239], v[232:233], 1.0 op_sel_hi:[1,1,0]
	v_cvt_pk_bf16_f32 v154, v138, v139
	v_cvt_pk_bf16_f32 v155, v140, v141
	v_cvt_pk_bf16_f32 v156, v150, v151
	v_cvt_pk_bf16_f32 v157, v152, v153
	v_cvt_pk_bf16_f32 v158, v184, v185
	v_cvt_pk_bf16_f32 v159, v186, v187
	v_cvt_pk_bf16_f32 v160, v240, v241
	v_cvt_pk_bf16_f32 v161, v242, v243
	ds_read_b128 v[18:21], v172
	ds_read_b128 v[2:5], v172 offset:64
	ds_read_b128 v[26:29], v172 offset:128
	ds_read_b128 v[10:13], v172 offset:192
	v_permlane16_swap_b32_e32 v154, v156
	v_permlane16_swap_b32_e32 v155, v157
	global_store_dwordx4 v228, v[154:157], s[60:61] offset:2048 nt
	v_permlane16_swap_b32_e32 v158, v160
	v_permlane16_swap_b32_e32 v159, v161
	global_store_dwordx4 v228, v[158:161], s[60:61] offset:2176 nt
	v_exp_f32_e32 v130, v22
	v_exp_f32_e32 v131, v23
	v_exp_f32_e32 v132, v24
	v_exp_f32_e32 v133, v25
	v_exp_f32_e32 v142, v6
	v_exp_f32_e32 v143, v7
	v_exp_f32_e32 v144, v8
	v_exp_f32_e32 v145, v9
	v_exp_f32_e32 v176, v30
	v_exp_f32_e32 v177, v31
	v_exp_f32_e32 v178, v32
	v_exp_f32_e32 v179, v33
	v_exp_f32_e32 v232, v14
	v_exp_f32_e32 v233, v15
	v_exp_f32_e32 v234, v16
	v_exp_f32_e32 v235, v17
	v_pk_fma_f32 v[130:131], v[130:131], -0.5, -0.5 op_sel_hi:[1,0,0]
	v_pk_fma_f32 v[132:133], v[132:133], -0.5, -0.5 op_sel_hi:[1,0,0]
	v_pk_fma_f32 v[142:143], v[142:143], -0.5, -0.5 op_sel_hi:[1,0,0]
	v_pk_fma_f32 v[144:145], v[144:145], -0.5, -0.5 op_sel_hi:[1,0,0]
	v_pk_fma_f32 v[176:177], v[176:177], -0.5, -0.5 op_sel_hi:[1,0,0]
	v_pk_fma_f32 v[178:179], v[178:179], -0.5, -0.5 op_sel_hi:[1,0,0]
	v_pk_fma_f32 v[232:233], v[232:233], -0.5, -0.5 op_sel_hi:[1,0,0]
	v_pk_fma_f32 v[234:235], v[234:235], -0.5, -0.5 op_sel_hi:[1,0,0]
	v_pk_mul_f32 v[134:135], v[130:131], v[132:133]
	v_pk_mul_f32 v[146:147], v[142:143], v[144:145]
	v_pk_mul_f32 v[180:181], v[176:177], v[178:179]
	v_pk_mul_f32 v[236:237], v[232:233], v[234:235]
	v_mul_f32_e32 v188, v134, v135
	v_mul_f32_e32 v190, v146, v147
	v_mul_f32_e32 v189, v180, v181
	v_mul_f32_e32 v191, v236, v237
	v_pk_mul_f32 v[192:193], v[188:189], v[190:191]
	v_mul_f32_e32 v174, v192, v193
	v_rcp_f32_e32 v173, v174
	v_pk_add_f32 v[164:165], v[164:165], v[22:23]
	v_pk_add_f32 v[164:165], v[164:165], v[24:25]
	v_pk_add_f32 v[164:165], v[164:165], v[6:7]
	v_pk_add_f32 v[164:165], v[164:165], v[8:9]
	v_pk_add_f32 v[164:165], v[164:165], v[30:31]
	v_pk_add_f32 v[164:165], v[164:165], v[32:33]
	v_pk_add_f32 v[164:165], v[164:165], v[14:15]
	v_pk_add_f32 v[164:165], v[164:165], v[16:17]
	v_pk_mul_f32 v[230:231], v[172:173], v[192:193] op_sel:[1,1] op_sel_hi:[1,0]
	v_pk_mul_f32 v[192:193], v[230:231], v[190:191]
	v_pk_mul_f32 v[190:191], v[230:231], v[188:189]
	v_pk_mul_f32 v[136:137], v[192:193], v[134:135] op_sel:[0,1] op_sel_hi:[0,0]
	v_pk_mul_f32 v[148:149], v[190:191], v[146:147] op_sel:[0,1] op_sel_hi:[0,0]
	v_pk_mul_f32 v[182:183], v[192:193], v[180:181] op_sel:[1,1] op_sel_hi:[1,0]
	v_pk_mul_f32 v[238:239], v[190:191], v[236:237] op_sel:[1,1] op_sel_hi:[1,0]
	v_pk_fma_f32 v[138:139], v[136:137], v[132:133], 1.0 op_sel_hi:[1,1,0]
	v_pk_fma_f32 v[140:141], v[136:137], v[130:131], 1.0 op_sel_hi:[1,1,0]
	v_pk_fma_f32 v[150:151], v[148:149], v[144:145], 1.0 op_sel_hi:[1,1,0]
	v_pk_fma_f32 v[152:153], v[148:149], v[142:143], 1.0 op_sel_hi:[1,1,0]
	v_pk_fma_f32 v[184:185], v[182:183], v[178:179], 1.0 op_sel_hi:[1,1,0]
	v_pk_fma_f32 v[186:187], v[182:183], v[176:177], 1.0 op_sel_hi:[1,1,0]
	v_pk_fma_f32 v[240:241], v[238:239], v[234:235], 1.0 op_sel_hi:[1,1,0]
	v_pk_fma_f32 v[242:243], v[238:239], v[232:233], 1.0 op_sel_hi:[1,1,0]
	v_cvt_pk_bf16_f32 v154, v138, v139
	v_cvt_pk_bf16_f32 v155, v140, v141
	v_cvt_pk_bf16_f32 v156, v150, v151
	v_cvt_pk_bf16_f32 v157, v152, v153
	v_cvt_pk_bf16_f32 v158, v184, v185
	v_cvt_pk_bf16_f32 v159, v186, v187
	v_cvt_pk_bf16_f32 v160, v240, v241
	v_cvt_pk_bf16_f32 v161, v242, v243
	ds_read_b128 v[22:25], v172 offset:512
	ds_read_b128 v[6:9], v172 offset:576
	ds_read_b128 v[30:33], v172 offset:640
	ds_read_b128 v[14:17], v172 offset:704
	v_permlane16_swap_b32_e32 v154, v156
	v_permlane16_swap_b32_e32 v155, v157
	global_store_dwordx4 v228, v[154:157], s[64:65] offset:2048 nt
	v_permlane16_swap_b32_e32 v158, v160
	v_permlane16_swap_b32_e32 v159, v161
	global_store_dwordx4 v228, v[158:161], s[64:65] offset:2176 nt
	v_log_f32_e32 v166, v162
	v_log_f32_e32 v170, v174
	v_add_f32_e32 v168, v164, v165
	v_mul_f32_e32 v168, 0xbeb17218, v168
	v_add_f32_e32 v166, v166, v170
	v_fmac_f32_e32 v168, 0x3f317218, v166
	v_mov_b32_e32 v169, v168
	s_nop 1
	v_permlane16_swap_b32_e32 v168, v169
	v_add_f32_e32 v168, v168, v169
	v_mov_b32_e32 v169, v168
	s_nop 1
	v_permlane32_swap_b32_e32 v168, v169
	v_add_f32_e32 v168, v168, v169
	s_mov_b64 exec, s[0:1]
	global_store_dword v229, v168, s[66:67] offset:576
	s_mov_b64 exec, -1
	s_bitcmp1_b32 s20, 12
	s_cbranch_scc0 .Lg1_noY
	s_barrier
